# re-measure: plan E + hand-written conversion routine in in-proj-0 conversion WGs + hand-written RG-LRU
# speedup vs baseline: 1.0146x; 1.0146x over previous
.LBB0_254:
	s_load_dwordx4 s[0:3], s[8:9], 0x138
	s_waitcnt lgkmcnt(0)
	s_mov_b64 s[4:5], s[0:1]
	s_cmp_lt_i32 s4, 3
	s_cselect_b64 s[0:1], -1, 0
	s_cmp_gt_i32 s5, 2
	s_cselect_b64 s[2:3], -1, 0
	s_and_b64 s[0:1], s[0:1], s[2:3]
	s_andn2_b64 vcc, exec, s[0:1]
	s_cbranch_vccnz .LBB0_356
	s_mov_b64 s[0:1], s[8:9]
	v_mbcnt_lo_u32_b32 v152, -1, 0
	v_mbcnt_hi_u32_b32 v152, -1, v152
	s_load_dword s38, s[8:9], 0x148
	s_add_u32 s2, s8, 0x148
	v_readlane_b32 s4, v243, 0
	s_addc_u32 s3, s9, 0
	v_readlane_b32 s5, v243, 1
	s_waitcnt lgkmcnt(0)
	s_sub_i32 s39, s38, 40
	s_cmp_lt_i32 s4, s39
	s_mov_b64 s[4:5], -1
	s_cbranch_scc1 .LBB0_276
	v_readlane_b32 s4, v243, 0
	s_sub_i32 s4, s4, s39
	s_lshl_b32 s4, s4, 3
	s_add_i32 s19, s4, s94
	s_mov_b32 s4, s19
	s_mov_b32 s5, 0x140
	s_mov_b32 s6, 0x3600
	s_waitcnt vmcnt(0)
	s_cmp_ge_u32 s4, s6
	s_cbranch_scc1 .Lp2c0_done
	v_readlane_b32 s8, v243, 7
	v_readlane_b32 s9, v243, 8
	s_load_dwordx2 s[10:11], s[8:9], 0x130
	s_load_dwordx2 s[12:13], s[8:9], 0xf8
	s_load_dwordx2 s[14:15], s[8:9], 0x108
	v_mbcnt_lo_u32_b32 v142, -1, 0
	v_mbcnt_hi_u32_b32 v142, -1, v142
	v_lshrrev_b32_e32 v143, 3, v142
	v_and_b32_e32 v142, 7, v142
	v_lshlrev_b32_e32 v136, 16, v143
	v_lshl_add_u32 v136, v142, 4, v136
	v_add_u32_e32 v137, 0x1000, v136
	v_add_u32_e32 v138, 0x2000, v136
	v_add_u32_e32 v139, 0x3000, v136
	v_lshlrev_b32_e32 v140, 12, v142
	v_lshl_add_u32 v140, v143, 4, v140
	v_mov_b32_e32 v141, 0x43e00000
	s_mov_b32 s28, 0xc3e00000
	s_waitcnt lgkmcnt(0)
	s_add_u32 s10, s10, 0x2900000
	s_addc_u32 s11, s11, 0
	s_lshr_b32 s22, s4, 8
	s_and_b32 s23, s4, 0xff
	s_and_b32 s27, s22, 1
	s_lshr_b32 s22, s22, 1
	s_cmp_eq_u32 s27, 0
	s_cselect_b64 s[16:17], s[12:13], s[14:15]
	s_add_i32 s22, s22, 20
	s_lshl_b32 s24, s22, 22
	s_lshr_b32 s25, s23, 5
	s_lshl_b32 s25, s25, 19
	s_and_b32 s26, s23, 31
	s_lshl_b32 s26, s26, 7
	s_add_i32 s24, s24, s25
	s_add_i32 s24, s24, s26
	s_add_u32 s16, s16, s24
	s_addc_u32 s17, s17, 0
	s_nop 0
	global_load_dwordx4 v[0:3], v136, s[16:17] nt
	global_load_dwordx4 v[4:7], v137, s[16:17] nt
	global_load_dwordx4 v[8:11], v138, s[16:17] nt
	global_load_dwordx4 v[12:15], v139, s[16:17] nt
	s_add_u32 s16, s16, 0x4000
	s_addc_u32 s17, s17, 0
	s_nop 0
	global_load_dwordx4 v[16:19], v136, s[16:17] nt
	global_load_dwordx4 v[20:23], v137, s[16:17] nt
	global_load_dwordx4 v[24:27], v138, s[16:17] nt
	global_load_dwordx4 v[28:31], v139, s[16:17] nt
	s_add_u32 s16, s16, 0x4000
	s_addc_u32 s17, s17, 0
	s_nop 0
	global_load_dwordx4 v[32:35], v136, s[16:17] nt
	global_load_dwordx4 v[36:39], v137, s[16:17] nt
	global_load_dwordx4 v[40:43], v138, s[16:17] nt
	global_load_dwordx4 v[44:47], v139, s[16:17] nt
	s_add_u32 s16, s16, 0x4000
	s_addc_u32 s17, s17, 0
	s_nop 0
	global_load_dwordx4 v[48:51], v136, s[16:17] nt
	global_load_dwordx4 v[52:55], v137, s[16:17] nt
	global_load_dwordx4 v[56:59], v138, s[16:17] nt
	global_load_dwordx4 v[60:63], v139, s[16:17] nt
	s_add_i32 s7, s4, s5
	s_cmp_lt_u32 s7, s6
	s_cbranch_scc0 .Lp2c0_p_last
	s_lshr_b32 s22, s7, 8
	s_and_b32 s23, s7, 0xff
	s_and_b32 s27, s22, 1
	s_lshr_b32 s22, s22, 1
	s_cmp_eq_u32 s27, 0
	s_cselect_b64 s[16:17], s[12:13], s[14:15]
	s_add_i32 s22, s22, 20
	s_lshl_b32 s24, s22, 22
	s_lshr_b32 s25, s23, 5
	s_lshl_b32 s25, s25, 19
	s_and_b32 s26, s23, 31
	s_lshl_b32 s26, s26, 7
	s_add_i32 s24, s24, s25
	s_add_i32 s24, s24, s26
	s_add_u32 s16, s16, s24
	s_addc_u32 s17, s17, 0
	s_nop 0
	global_load_dwordx4 v[64:67], v136, s[16:17] nt
	global_load_dwordx4 v[68:71], v137, s[16:17] nt
	global_load_dwordx4 v[72:75], v138, s[16:17] nt
	global_load_dwordx4 v[76:79], v139, s[16:17] nt
	s_add_u32 s16, s16, 0x4000
	s_addc_u32 s17, s17, 0
	s_nop 0
	global_load_dwordx4 v[80:83], v136, s[16:17] nt
	global_load_dwordx4 v[84:87], v137, s[16:17] nt
	global_load_dwordx4 v[88:91], v138, s[16:17] nt
	global_load_dwordx4 v[92:95], v139, s[16:17] nt
	s_add_u32 s16, s16, 0x4000
	s_addc_u32 s17, s17, 0
	s_nop 0
	global_load_dwordx4 v[96:99], v136, s[16:17] nt
	global_load_dwordx4 v[100:103], v137, s[16:17] nt
	global_load_dwordx4 v[104:107], v138, s[16:17] nt
	global_load_dwordx4 v[108:111], v139, s[16:17] nt
	s_add_u32 s16, s16, 0x4000
	s_addc_u32 s17, s17, 0
	s_nop 0
	global_load_dwordx4 v[112:115], v136, s[16:17] nt
	global_load_dwordx4 v[116:119], v137, s[16:17] nt
	global_load_dwordx4 v[120:123], v138, s[16:17] nt
	global_load_dwordx4 v[124:127], v139, s[16:17] nt
	s_waitcnt vmcnt(16)
	s_branch .Lp2c0_p_st

.Lp2c0_A_st:
	s_lshr_b32 s22, s4, 8
	s_and_b32 s23, s4, 0xff
	s_and_b32 s27, s22, 1
	s_lshr_b32 s22, s22, 1
	s_add_i32 s22, s22, 20
	s_mul_i32 s24, s22, 0x300000
	s_lshr_b32 s25, s23, 5
	s_lshl_b32 s25, s25, 7
	s_add_i32 s24, s24, s25
	s_and_b32 s26, s23, 31
	s_lshr_b32 s25, s26, 2
	s_lshl_b32 s25, s25, 18
	s_add_i32 s24, s24, s25
	s_lshl_b32 s25, s27, 17
	s_add_i32 s24, s24, s25
	s_and_b32 s25, s26, 3
	s_lshl_b32 s25, s25, 15
	s_add_i32 s24, s24, s25
	s_add_u32 s20, s10, s24
	s_addc_u32 s21, s11, 0
	v_mul_f32_e32 v0, 0x42000000, v0
	v_mul_f32_e32 v4, 0x42000000, v4
	v_mul_f32_e32 v8, 0x42000000, v8
	v_mul_f32_e32 v12, 0x42000000, v12
	v_mul_f32_e32 v16, 0x42000000, v16
	v_mul_f32_e32 v20, 0x42000000, v20
	v_mul_f32_e32 v24, 0x42000000, v24
	v_mul_f32_e32 v28, 0x42000000, v28
	v_mul_f32_e32 v32, 0x42000000, v32
	v_mul_f32_e32 v36, 0x42000000, v36
	v_mul_f32_e32 v40, 0x42000000, v40
	v_mul_f32_e32 v44, 0x42000000, v44
	v_mul_f32_e32 v48, 0x42000000, v48
	v_mul_f32_e32 v52, 0x42000000, v52
	v_mul_f32_e32 v56, 0x42000000, v56
	v_mul_f32_e32 v60, 0x42000000, v60
	v_med3_f32 v0, v0, s28, v141
	v_med3_f32 v4, v4, s28, v141
	v_med3_f32 v8, v8, s28, v141
	v_med3_f32 v12, v12, s28, v141
	v_med3_f32 v16, v16, s28, v141
	v_med3_f32 v20, v20, s28, v141
	v_med3_f32 v24, v24, s28, v141
	v_med3_f32 v28, v28, s28, v141
	v_med3_f32 v32, v32, s28, v141
	v_med3_f32 v36, v36, s28, v141
	v_med3_f32 v40, v40, s28, v141
	v_med3_f32 v44, v44, s28, v141
	v_med3_f32 v48, v48, s28, v141
	v_med3_f32 v52, v52, s28, v141
	v_med3_f32 v56, v56, s28, v141
	v_med3_f32 v60, v60, s28, v141
	v_cvt_pk_fp8_f32 v128, v0, v4
	v_cvt_pk_fp8_f32 v129, v16, v20
	v_cvt_pk_fp8_f32 v130, v32, v36
	v_cvt_pk_fp8_f32 v131, v48, v52
	v_cvt_pk_fp8_f32 v128, v8, v12 op_sel:[0,0,1]
	v_cvt_pk_fp8_f32 v129, v24, v28 op_sel:[0,0,1]
	v_cvt_pk_fp8_f32 v130, v40, v44 op_sel:[0,0,1]
	v_cvt_pk_fp8_f32 v131, v56, v60 op_sel:[0,0,1]
	s_nop 0
	global_store_dwordx4 v140, v[128:131], s[20:21]
	v_mul_f32_e32 v1, 0x42000000, v1
	v_mul_f32_e32 v5, 0x42000000, v5
	v_mul_f32_e32 v9, 0x42000000, v9
	v_mul_f32_e32 v13, 0x42000000, v13
	v_mul_f32_e32 v17, 0x42000000, v17
	v_mul_f32_e32 v21, 0x42000000, v21
	v_mul_f32_e32 v25, 0x42000000, v25
	v_mul_f32_e32 v29, 0x42000000, v29
	v_mul_f32_e32 v33, 0x42000000, v33
	v_mul_f32_e32 v37, 0x42000000, v37
	v_mul_f32_e32 v41, 0x42000000, v41
	v_mul_f32_e32 v45, 0x42000000, v45
	v_mul_f32_e32 v49, 0x42000000, v49
	v_mul_f32_e32 v53, 0x42000000, v53
	v_mul_f32_e32 v57, 0x42000000, v57
	v_mul_f32_e32 v61, 0x42000000, v61
	v_med3_f32 v1, v1, s28, v141
	v_med3_f32 v5, v5, s28, v141
	v_med3_f32 v9, v9, s28, v141
	v_med3_f32 v13, v13, s28, v141
	v_med3_f32 v17, v17, s28, v141
	v_med3_f32 v21, v21, s28, v141
	v_med3_f32 v25, v25, s28, v141
	v_med3_f32 v29, v29, s28, v141
	v_med3_f32 v33, v33, s28, v141
	v_med3_f32 v37, v37, s28, v141
	v_med3_f32 v41, v41, s28, v141
	v_med3_f32 v45, v45, s28, v141
	v_med3_f32 v49, v49, s28, v141
	v_med3_f32 v53, v53, s28, v141
	v_med3_f32 v57, v57, s28, v141
	v_med3_f32 v61, v61, s28, v141
	v_cvt_pk_fp8_f32 v132, v1, v5
	v_cvt_pk_fp8_f32 v133, v17, v21
	v_cvt_pk_fp8_f32 v134, v33, v37
	v_cvt_pk_fp8_f32 v135, v49, v53
	v_cvt_pk_fp8_f32 v132, v9, v13 op_sel:[0,0,1]
	v_cvt_pk_fp8_f32 v133, v25, v29 op_sel:[0,0,1]
	v_cvt_pk_fp8_f32 v134, v41, v45 op_sel:[0,0,1]
	v_cvt_pk_fp8_f32 v135, v57, v61 op_sel:[0,0,1]
	s_nop 0
	global_store_dwordx4 v140, v[132:135], s[20:21] offset:1024
	v_mul_f32_e32 v2, 0x42000000, v2
	v_mul_f32_e32 v6, 0x42000000, v6
	v_mul_f32_e32 v10, 0x42000000, v10
	v_mul_f32_e32 v14, 0x42000000, v14
	v_mul_f32_e32 v18, 0x42000000, v18
	v_mul_f32_e32 v22, 0x42000000, v22
	v_mul_f32_e32 v26, 0x42000000, v26
	v_mul_f32_e32 v30, 0x42000000, v30
	v_mul_f32_e32 v34, 0x42000000, v34
	v_mul_f32_e32 v38, 0x42000000, v38
	v_mul_f32_e32 v42, 0x42000000, v42
	v_mul_f32_e32 v46, 0x42000000, v46
	v_mul_f32_e32 v50, 0x42000000, v50
	v_mul_f32_e32 v54, 0x42000000, v54
	v_mul_f32_e32 v58, 0x42000000, v58
	v_mul_f32_e32 v62, 0x42000000, v62
	v_med3_f32 v2, v2, s28, v141
	v_med3_f32 v6, v6, s28, v141
	v_med3_f32 v10, v10, s28, v141
	v_med3_f32 v14, v14, s28, v141
	v_med3_f32 v18, v18, s28, v141
	v_med3_f32 v22, v22, s28, v141
	v_med3_f32 v26, v26, s28, v141
	v_med3_f32 v30, v30, s28, v141
	v_med3_f32 v34, v34, s28, v141
	v_med3_f32 v38, v38, s28, v141
	v_med3_f32 v42, v42, s28, v141
	v_med3_f32 v46, v46, s28, v141
	v_med3_f32 v50, v50, s28, v141
	v_med3_f32 v54, v54, s28, v141
	v_med3_f32 v58, v58, s28, v141
	v_med3_f32 v62, v62, s28, v141
	v_cvt_pk_fp8_f32 v128, v2, v6
	v_cvt_pk_fp8_f32 v129, v18, v22
	v_cvt_pk_fp8_f32 v130, v34, v38
	v_cvt_pk_fp8_f32 v131, v50, v54
	v_cvt_pk_fp8_f32 v128, v10, v14 op_sel:[0,0,1]
	v_cvt_pk_fp8_f32 v129, v26, v30 op_sel:[0,0,1]
	v_cvt_pk_fp8_f32 v130, v42, v46 op_sel:[0,0,1]
	v_cvt_pk_fp8_f32 v131, v58, v62 op_sel:[0,0,1]
	s_nop 0
	global_store_dwordx4 v140, v[128:131], s[20:21] offset:2048
	v_mul_f32_e32 v3, 0x42000000, v3
	v_mul_f32_e32 v7, 0x42000000, v7
	v_mul_f32_e32 v11, 0x42000000, v11
	v_mul_f32_e32 v15, 0x42000000, v15
	v_mul_f32_e32 v19, 0x42000000, v19
	v_mul_f32_e32 v23, 0x42000000, v23
	v_mul_f32_e32 v27, 0x42000000, v27
	v_mul_f32_e32 v31, 0x42000000, v31
	v_mul_f32_e32 v35, 0x42000000, v35
	v_mul_f32_e32 v39, 0x42000000, v39
	v_mul_f32_e32 v43, 0x42000000, v43
	v_mul_f32_e32 v47, 0x42000000, v47
	v_mul_f32_e32 v51, 0x42000000, v51
	v_mul_f32_e32 v55, 0x42000000, v55
	v_mul_f32_e32 v59, 0x42000000, v59
	v_mul_f32_e32 v63, 0x42000000, v63
	v_med3_f32 v3, v3, s28, v141
	v_med3_f32 v7, v7, s28, v141
	v_med3_f32 v11, v11, s28, v141
	v_med3_f32 v15, v15, s28, v141
	v_med3_f32 v19, v19, s28, v141
	v_med3_f32 v23, v23, s28, v141
	v_med3_f32 v27, v27, s28, v141
	v_med3_f32 v31, v31, s28, v141
	v_med3_f32 v35, v35, s28, v141
	v_med3_f32 v39, v39, s28, v141
	v_med3_f32 v43, v43, s28, v141
	v_med3_f32 v47, v47, s28, v141
	v_med3_f32 v51, v51, s28, v141
	v_med3_f32 v55, v55, s28, v141
	v_med3_f32 v59, v59, s28, v141
	v_med3_f32 v63, v63, s28, v141
	v_cvt_pk_fp8_f32 v132, v3, v7
	v_cvt_pk_fp8_f32 v133, v19, v23
	v_cvt_pk_fp8_f32 v134, v35, v39
	v_cvt_pk_fp8_f32 v135, v51, v55
	v_cvt_pk_fp8_f32 v132, v11, v15 op_sel:[0,0,1]
	v_cvt_pk_fp8_f32 v133, v27, v31 op_sel:[0,0,1]
	v_cvt_pk_fp8_f32 v134, v43, v47 op_sel:[0,0,1]
	v_cvt_pk_fp8_f32 v135, v59, v63 op_sel:[0,0,1]
	s_nop 0
	global_store_dwordx4 v140, v[132:135], s[20:21] offset:3072
	s_cmp_ge_u32 s7, s6
	s_cbranch_scc1 .Lp2c0_done
	s_mov_b32 s4, s7
	s_branch .Lp2c0_loop
.Lp2c0_done:
.LBB0_275:
	s_mov_b64 s[4:5], 0
